# v66 + P10 boundary search: per-row suffix sums by a DPP prefix scan (row_shr/row_bcast) instead of 6 ds_bpermute round trips
# baseline (speedup 1.0000x reference)
.LBB0_1146:
	v_add_u32_e32 v4, s24, v179
	ds_read_b128 v[0:3], v4
	ds_read_b128 v[4:7], v4 offset:16
	s_waitcnt lgkmcnt(1)
	v_add_u32_e32 v8, v1, v0
	v_add3_u32 v8, v8, v2, v3
	s_waitcnt lgkmcnt(0)
	v_add3_u32 v8, v8, v4, v5
	v_add3_u32 v8, v8, v6, v7
	v_mov_b32_e32 v9, v8
	s_nop 1
	v_add_u32_dpp v9, v9, v9 row_shr:1 row_mask:0xf bank_mask:0xf bound_ctrl:0
	s_nop 1
	v_add_u32_dpp v9, v9, v9 row_shr:2 row_mask:0xf bank_mask:0xf bound_ctrl:0
	s_nop 1
	v_add_u32_dpp v9, v9, v9 row_shr:4 row_mask:0xf bank_mask:0xf bound_ctrl:0
	s_nop 1
	v_add_u32_dpp v9, v9, v9 row_shr:8 row_mask:0xf bank_mask:0xf bound_ctrl:0
	s_nop 1
	v_add_u32_dpp v9, v9, v9 row_bcast:15 row_mask:0xa bank_mask:0xf
	s_nop 1
	v_add_u32_dpp v9, v9, v9 row_bcast:31 row_mask:0xc bank_mask:0xf
	s_nop 1
	v_readlane_b32 s0, v9, 63
	s_nop 1
	v_sub_u32_e32 v10, s0, v9
	v_add_u32_e32 v10, v10, v8
	v_sub_u32_e32 v9, v10, v8
	v_cmp_gt_i32_e32 vcc, s48, v9
	v_cmp_lt_i32_e64 s[50:51], s74, v10
	s_and_b64 s[0:1], s[50:51], vcc
	s_and_saveexec_b64 s[50:51], s[0:1]
	s_cbranch_execz .LBB0_1145
	v_add_u32_e32 v10, v9, v7
	v_cmp_gt_i32_e32 vcc, s48, v10
	s_mov_b64 s[54:55], -1
	s_mov_b64 s[58:59], -1
	v_mov_b32_e32 v8, v172
	v_mov_b32_e32 v7, v9
	s_and_saveexec_b64 s[56:57], vcc
	s_cbranch_execz .LBB0_1151
	v_add_u32_e32 v9, v10, v6
	v_cmp_lt_i32_e32 vcc, s74, v9
	v_mov_b32_e32 v7, 0
	s_mov_b64 s[58:59], 0
	v_mov_b32_e32 v8, 0
	s_and_saveexec_b64 s[0:1], vcc
	s_mov_b64 s[58:59], exec
	v_mov_b32_e32 v7, v10
	v_mov_b32_e32 v8, v173
	v_mov_b32_e32 v9, v10
	s_or_b64 exec, exec, s[0:1]
	s_orn2_b64 s[58:59], s[58:59], exec

.LBB0_1201:
	v_add_u32_e32 v4, s24, v179
	ds_read_b128 v[0:3], v4
	ds_read_b128 v[4:7], v4 offset:16
	s_waitcnt lgkmcnt(1)
	v_add_u32_e32 v8, v1, v0
	v_add3_u32 v8, v8, v2, v3
	s_waitcnt lgkmcnt(0)
	v_add3_u32 v8, v8, v4, v5
	v_add3_u32 v8, v8, v6, v7
	v_mov_b32_e32 v9, v8
	s_nop 1
	v_add_u32_dpp v9, v9, v9 row_shr:1 row_mask:0xf bank_mask:0xf bound_ctrl:0
	s_nop 1
	v_add_u32_dpp v9, v9, v9 row_shr:2 row_mask:0xf bank_mask:0xf bound_ctrl:0
	s_nop 1
	v_add_u32_dpp v9, v9, v9 row_shr:4 row_mask:0xf bank_mask:0xf bound_ctrl:0
	s_nop 1
	v_add_u32_dpp v9, v9, v9 row_shr:8 row_mask:0xf bank_mask:0xf bound_ctrl:0
	s_nop 1
	v_add_u32_dpp v9, v9, v9 row_bcast:15 row_mask:0xa bank_mask:0xf
	s_nop 1
	v_add_u32_dpp v9, v9, v9 row_bcast:31 row_mask:0xc bank_mask:0xf
	s_nop 1
	v_readlane_b32 s0, v9, 63
	s_nop 1
	v_sub_u32_e32 v10, s0, v9
	v_add_u32_e32 v10, v10, v8
	v_sub_u32_e32 v9, v10, v8
	v_cmp_gt_i32_e32 vcc, s48, v9
	v_cmp_lt_i32_e64 s[50:51], s74, v10
	s_and_b64 s[0:1], s[50:51], vcc
	s_and_saveexec_b64 s[50:51], s[0:1]
	s_cbranch_execz .LBB0_1200
	v_add_u32_e32 v10, v9, v7
	v_cmp_gt_i32_e32 vcc, s48, v10
	s_mov_b64 s[52:53], -1
	s_mov_b64 s[56:57], -1
	v_mov_b32_e32 v8, v172
	v_mov_b32_e32 v7, v9
	s_and_saveexec_b64 s[54:55], vcc
	s_cbranch_execz .LBB0_1206
	v_add_u32_e32 v9, v10, v6
	v_cmp_lt_i32_e32 vcc, s74, v9
	v_mov_b32_e32 v7, 0
	s_mov_b64 s[56:57], 0
	v_mov_b32_e32 v8, 0
	s_and_saveexec_b64 s[0:1], vcc
	s_mov_b64 s[56:57], exec
	v_mov_b32_e32 v7, v10
	v_mov_b32_e32 v8, v173
	v_mov_b32_e32 v9, v10
	s_or_b64 exec, exec, s[0:1]
	s_orn2_b64 s[56:57], s[56:57], exec
